# boundary decouple v2: counted wait at K-loop entry (stores+prefetch), trip-0 first two vmcnt waits skipped for non-first units, 4 GEMM phases
# baseline (speedup 1.0000x reference)
; #define LAS __attribute__((address_space(3)))
; DI const char* sptr(const char* p) { const unsigned long long v = (unsigned long long)p; const unsigned lo = __builtin_amdgcn_readfirstlane((unsigned)v), hi = __builtin_amdgcn_readfirstlane((unsigned)(v >> 32)); return (const char*)(((unsigned long long)hi << 32) | lo); }
; template <class Epi, bool GATHER, bool EXPERT, bool FP8>
; DI void gemm_phase(LAS unsigned char* lds, const Gemm g, const StaticOrder& S, const Epi& E) {
;     ...
;         const char* nA = sptr(has_next ? (const char*)g.A + (GATHER ? (size_t)0 : (size_t)nxt.pm * tstep) : cA);
;         const char* nB = sptr(has_next ? (const char*)g.Bt + (size_t)nxt.e * g.estride + (size_t)nxt.pn * tstep : cB);
;         if (GATHER && has_next) {
;             int t2_ = threadIdx.x; asm volatile("" : "+v"(t2_));
; #pragma unroll
;             for (int i_ = 0; i_ < 2; ++i_) { int R_, C_; stage_rc(t2_ * 16 + i_ * 8192, R_, C_);
; #pragma unroll
;                 for (int h_ = 0; h_ < 2; ++h_) __builtin_amdgcn_global_load_lds((const unsigned*)(g.rowtok + nxt.pm * 256 + h_ * 128 + R_), (LAS unsigned*)(stash + (h_ * 2 + i_) * 2048), 4, 0, 0); }
;         }
;         int C0x2 = 0, C1x2 = 0; const LAS unsigned* sp = nullptr;
;         if (GATHER) { int t2_ = threadIdx.x; asm volatile("" : "+v"(t2_)); int R0_, C0_, R1_, C1_; stage_rc(t2_ * 16, R0_, C0_); stage_rc(t2_ * 16 + 8192, R1_, C1_); C0x2 = C0_ * 2; C1x2 = C1_ * 2;
;             sp = (const LAS unsigned*)(stash + (t2_ & 63) * 4); }
;         asm volatile(".p2align 8" ::: "memory");
; #pragma unroll 1
;         for (int t = 0; t < nt; t += 2) {
;             const bool last = (t == nt - 2);
;             const char* a1 = cA + (size_t)(t + 1) * kstep;
;             const char* a2 = last ? nA : cA + (size_t)(t + 2) * kstep; const char* b2 = last ? nB : cB + (size_t)(t + 2) * kstep;
;             const char* a3 = a2 + kstep; const char* b3 = b2 + kstep;
;     ...
;         for (int a = 0; a < 2; ++a)
; #pragma unroll
;             for (int b = 0; b < 2; ++b)
; #pragma unroll
;                 for (int m = 0; m < 4; ++m)
; #pragma unroll
;                     for (int n = 0; n < 2; ++n) acc[a][b][m][n] = (f32x4){0.f, 0.f, 0.f, 0.f};
.LBB0_114:
	s_ashr_i32 s41, s40, 31
	s_lshl_b64 s[0:1], s[40:41], 20
	s_add_u32 s5, s49, s0
	s_addc_u32 s15, s50, s1
	s_and_b64 s[0:1], s[2:3], exec
	s_cselect_b32 s42, s5, s6
	s_cselect_b32 s43, s15, s7
	s_ashr_i32 s39, s38, 31
	s_lshl_b64 s[0:1], s[38:39], 20
	s_add_u32 s5, s51, s0
	s_addc_u32 s15, s52, s1
	s_and_b64 s[0:1], s[2:3], exec
	s_cselect_b32 s44, s5, s8
	s_cselect_b32 s45, s15, s9
	s_add_u32 s5, s8, 0x100
	.p2align 8
	s_addc_u32 s15, s9, 0
	s_add_u32 s6, s6, 0x80
	v_mov_b32_e32 v2, 0
	s_addc_u32 s7, s7, 0
	s_mov_b32 s18, -2
	v_mov_b32_e32 v3, v2
	v_mov_b32_e32 v4, v2
	v_mov_b32_e32 v5, v2
	v_mov_b32_e32 v6, v2
	v_mov_b32_e32 v7, v2
	v_mov_b32_e32 v8, v2
	v_mov_b32_e32 v9, v2
	v_mov_b32_e32 v10, v2
	v_mov_b32_e32 v11, v2
	v_mov_b32_e32 v12, v2
	v_mov_b32_e32 v13, v2
	v_mov_b32_e32 v18, v2
	v_mov_b32_e32 v19, v2
	v_mov_b32_e32 v20, v2
	v_mov_b32_e32 v21, v2
	v_mov_b32_e32 v26, v2
	v_mov_b32_e32 v27, v2
	v_mov_b32_e32 v28, v2
	v_mov_b32_e32 v29, v2
	s_waitcnt vmcnt(0)
	v_mov_b32_e32 v34, v2
	v_mov_b32_e32 v35, v2
	v_mov_b32_e32 v36, v2
	v_mov_b32_e32 v37, v2
	v_mov_b32_e32 v42, v2
	v_mov_b32_e32 v43, v2
	v_mov_b32_e32 v44, v2
	v_mov_b32_e32 v45, v2
	v_mov_b32_e32 v50, v2
	v_mov_b32_e32 v51, v2
	v_mov_b32_e32 v52, v2
	v_mov_b32_e32 v53, v2
	v_mov_b32_e32 v14, v2
	v_mov_b32_e32 v15, v2
	v_mov_b32_e32 v16, v2
	v_mov_b32_e32 v17, v2
	v_mov_b32_e32 v22, v2
	v_mov_b32_e32 v23, v2
	v_mov_b32_e32 v24, v2
	v_mov_b32_e32 v25, v2
	v_mov_b32_e32 v30, v2
	v_mov_b32_e32 v31, v2
	v_mov_b32_e32 v32, v2
	v_mov_b32_e32 v33, v2
	v_mov_b32_e32 v38, v2
	v_mov_b32_e32 v39, v2
	v_mov_b32_e32 v40, v2
	v_mov_b32_e32 v41, v2
	v_mov_b32_e32 v46, v2
	v_mov_b32_e32 v47, v2
	v_mov_b32_e32 v48, v2
	v_mov_b32_e32 v49, v2
	v_mov_b32_e32 v54, v2
	v_mov_b32_e32 v55, v2
	v_mov_b32_e32 v56, v2
	v_mov_b32_e32 v57, v2
	v_mov_b32_e32 v58, v2
	v_mov_b32_e32 v59, v2
	v_mov_b32_e32 v60, v2
	v_mov_b32_e32 v61, v2
	v_mov_b32_e32 v62, v2
	v_mov_b32_e32 v63, v2
	v_mov_b32_e32 v64, v2
	v_mov_b32_e32 v65, v2
	v_mov_b32_e32 v66, v2
	v_mov_b32_e32 v67, v2
	v_mov_b32_e32 v68, v2
	v_mov_b32_e32 v69, v2
	v_mov_b32_e32 v70, v2
	v_mov_b32_e32 v71, v2
	v_mov_b32_e32 v72, v2
	v_mov_b32_e32 v73, v2
	v_mov_b32_e32 v74, v2
	v_mov_b32_e32 v75, v2
	v_mov_b32_e32 v76, v2
	v_mov_b32_e32 v77, v2
	v_mov_b32_e32 v82, v2
	v_mov_b32_e32 v83, v2
	v_mov_b32_e32 v84, v2
	v_mov_b32_e32 v85, v2
	v_mov_b32_e32 v90, v2
	v_mov_b32_e32 v91, v2
	v_mov_b32_e32 v92, v2
	v_mov_b32_e32 v93, v2
	v_mov_b32_e32 v98, v2
	v_mov_b32_e32 v99, v2
	v_mov_b32_e32 v100, v2
	v_mov_b32_e32 v101, v2
	v_mov_b32_e32 v106, v2
	v_mov_b32_e32 v107, v2
	v_mov_b32_e32 v108, v2
	v_mov_b32_e32 v109, v2
	v_mov_b32_e32 v114, v2
	v_mov_b32_e32 v115, v2
	v_mov_b32_e32 v116, v2
	v_mov_b32_e32 v117, v2
	v_mov_b32_e32 v78, v2
	v_mov_b32_e32 v79, v2
	v_mov_b32_e32 v80, v2
	v_mov_b32_e32 v81, v2
	v_mov_b32_e32 v86, v2
	v_mov_b32_e32 v87, v2
	v_mov_b32_e32 v88, v2
	v_mov_b32_e32 v89, v2
	v_mov_b32_e32 v94, v2
	v_mov_b32_e32 v95, v2
	v_mov_b32_e32 v96, v2
	v_mov_b32_e32 v97, v2
	v_mov_b32_e32 v102, v2
	v_mov_b32_e32 v103, v2
	v_mov_b32_e32 v104, v2
	v_mov_b32_e32 v105, v2
	v_mov_b32_e32 v110, v2
	v_mov_b32_e32 v111, v2
	v_mov_b32_e32 v112, v2
	v_mov_b32_e32 v113, v2
	v_mov_b32_e32 v118, v2
	v_mov_b32_e32 v119, v2
	v_mov_b32_e32 v120, v2
	v_mov_b32_e32 v121, v2
	v_mov_b32_e32 v122, v2
	v_mov_b32_e32 v123, v2
	v_mov_b32_e32 v124, v2
	v_mov_b32_e32 v125, v2
	v_mov_b32_e32 v126, v2
	v_mov_b32_e32 v127, v2
	v_mov_b32_e32 v128, v2
	v_mov_b32_e32 v129, v2
	s_cmp_gt_u32 s48, 1
	s_cselect_b32 s32, -2, 1
	s_waitcnt vmcnt(16)

; #define LAS __attribute__((address_space(3)))
; template <class Epi, bool GATHER, bool EXPERT, bool FP8>
; DI void gemm_phase(LAS unsigned char* lds, const Gemm g, const StaticOrder& S, const Epi& E) {
;     ...
;         int C0x2 = 0, C1x2 = 0; const LAS unsigned* sp = nullptr;
;         if (GATHER) { int t2_ = threadIdx.x; asm volatile("" : "+v"(t2_)); int R0_, C0_, R1_, C1_; stage_rc(t2_ * 16, R0_, C0_); stage_rc(t2_ * 16 + 8192, R1_, C1_); C0x2 = C0_ * 2; C1x2 = C1_ * 2;
;             sp = (const LAS unsigned*)(stash + (t2_ & 63) * 4); }
;         asm volatile(".p2align 8" ::: "memory");
; #pragma unroll 1
;         for (int t = 0; t < nt; t += 2) {
;             const bool last = (t == nt - 2);
;             const char* a1 = cA + (size_t)(t + 1) * kstep;
;             const char* a2 = last ? nA : cA + (size_t)(t + 2) * kstep; const char* b2 = last ? nB : cB + (size_t)(t + 2) * kstep;
;             const char* a3 = a2 + kstep; const char* b3 = b2 + kstep;
;     ...
;         for (int a = 0; a < 2; ++a)
; #pragma unroll
;             for (int b = 0; b < 2; ++b)
; #pragma unroll
;                 for (int m = 0; m < 4; ++m)
; #pragma unroll
;                     for (int n = 0; n < 2; ++n) acc[a][b][m][n] = (f32x4){0.f, 0.f, 0.f, 0.f};
.LBB0_1083:
	v_mov_b32_e32 v2, v0
	s_add_u32 s25, s36, 0x100
	v_bfe_i32 v5, v2, 27, 1
	v_lshlrev_b32_e32 v3, 4, v2
	v_lshrrev_b32_e32 v5, 22, v5
	v_add_u32_e32 v5, v3, v5
	v_and_b32_e32 v5, 0xfffffc00, v5
	v_sub_u32_e32 v5, v3, v5
	v_lshrrev_b32_e32 v6, 4, v5
	v_bitop3_b32 v6, v6, v5, 32 bitop3:0x6c
	v_ashrrev_i32_e32 v5, 31, v5
	v_lshrrev_b32_e32 v5, 26, v5
	v_add_u32_e32 v5, v6, v5
	v_and_b32_e32 v5, 0xc0, v5
	v_add_u32_e32 v3, 0x2000, v3
	v_sub_u32_e32 v5, v6, v5
	v_ashrrev_i32_e32 v6, 31, v3
	v_lshrrev_b32_e32 v6, 22, v6
	v_add_u32_e32 v6, v3, v6
	v_ashrrev_i32_e32 v6, 10, v6
	v_mul_i32_i24_e32 v7, 0x400, v6
	v_sub_u32_e32 v3, v3, v7
	v_lshrrev_b32_e32 v7, 4, v3
	v_bitop3_b32 v7, v7, v3, 32 bitop3:0x6c
	v_ashrrev_i32_e32 v3, 31, v3
	v_lshrrev_b32_e32 v3, 26, v3
	v_add_u32_e32 v3, v7, v3
	v_ashrrev_i32_e32 v4, 31, v2
	v_and_b32_e32 v3, 0xc0, v3
	v_lshrrev_b32_e32 v4, 26, v4
	v_sub_u32_e32 v3, v7, v3
	v_add_u32_e32 v4, v2, v4
	v_lshlrev_b32_e32 v6, 5, v6
	v_ashrrev_i16_sdwa v3, v1, sext(v3) dst_sel:DWORD dst_unused:UNUSED_PAD src0_sel:DWORD src1_sel:BYTE_0
	v_lshrrev_b32_e32 v4, 1, v4
	v_ashrrev_i16_sdwa v5, v1, sext(v5) dst_sel:DWORD dst_unused:UNUSED_PAD src0_sel:DWORD src1_sel:BYTE_0
	v_and_b32_e32 v6, 32, v6
	v_bfe_i32 v3, v3, 0, 16
	v_lshlrev_b32_e32 v2, 2, v2
	.p2align 8
	s_addc_u32 s72, s37, 0
	v_and_b32_e32 v4, 32, v4
	v_bfe_i32 v5, v5, 0, 16
	v_add_lshl_u32 v131, v6, v3, 1
	v_and_b32_e32 v3, 0xfc, v2
	s_add_u32 s36, s0, 0x80
	v_mov_b32_e32 v2, 0
	v_add_lshl_u32 v130, v4, v5, 1
	s_addc_u32 s37, s1, 0
	s_mov_b32 s0, -2
	v_add_u32_e32 v132, s57, v3
	v_mov_b32_e32 v3, v2
	v_mov_b32_e32 v4, v2
	v_mov_b32_e32 v5, v2
	v_mov_b32_e32 v10, v2
	v_mov_b32_e32 v11, v2
	v_mov_b32_e32 v12, v2
	v_mov_b32_e32 v13, v2
	v_mov_b32_e32 v18, v2
	v_mov_b32_e32 v19, v2
	v_mov_b32_e32 v20, v2
	v_mov_b32_e32 v21, v2
	v_mov_b32_e32 v26, v2
	v_mov_b32_e32 v27, v2
	v_mov_b32_e32 v28, v2
	v_mov_b32_e32 v29, v2
	v_mov_b32_e32 v34, v2
	v_mov_b32_e32 v35, v2
	v_mov_b32_e32 v36, v2
	v_mov_b32_e32 v37, v2
	v_mov_b32_e32 v42, v2
	v_mov_b32_e32 v43, v2
	v_mov_b32_e32 v44, v2
	v_mov_b32_e32 v45, v2
	v_mov_b32_e32 v50, v2
	v_mov_b32_e32 v51, v2
	v_mov_b32_e32 v52, v2
	v_mov_b32_e32 v53, v2
	v_mov_b32_e32 v58, v2
	v_mov_b32_e32 v59, v2
	v_mov_b32_e32 v60, v2
	v_mov_b32_e32 v61, v2
	v_mov_b32_e32 v6, v2
	v_mov_b32_e32 v7, v2
	v_mov_b32_e32 v8, v2
	v_mov_b32_e32 v9, v2
	v_mov_b32_e32 v14, v2
	v_mov_b32_e32 v15, v2
	v_mov_b32_e32 v16, v2
	v_mov_b32_e32 v17, v2
	v_mov_b32_e32 v22, v2
	v_mov_b32_e32 v23, v2
	v_mov_b32_e32 v24, v2
	v_mov_b32_e32 v25, v2
	v_mov_b32_e32 v30, v2
	v_mov_b32_e32 v31, v2
	v_mov_b32_e32 v32, v2
	v_mov_b32_e32 v33, v2
	v_mov_b32_e32 v38, v2
	v_mov_b32_e32 v39, v2
	v_mov_b32_e32 v40, v2
	v_mov_b32_e32 v41, v2
	v_mov_b32_e32 v46, v2
	v_mov_b32_e32 v47, v2
	v_mov_b32_e32 v48, v2
	v_mov_b32_e32 v49, v2
	v_mov_b32_e32 v54, v2
	v_mov_b32_e32 v55, v2
	v_mov_b32_e32 v56, v2
	v_mov_b32_e32 v57, v2
	v_mov_b32_e32 v62, v2
	v_mov_b32_e32 v63, v2
	v_mov_b32_e32 v64, v2
	v_mov_b32_e32 v65, v2
	v_mov_b32_e32 v66, v2
	v_mov_b32_e32 v67, v2
	v_mov_b32_e32 v68, v2
	v_mov_b32_e32 v69, v2
	v_mov_b32_e32 v74, v2
	v_mov_b32_e32 v75, v2
	v_mov_b32_e32 v76, v2
	v_mov_b32_e32 v77, v2
	v_mov_b32_e32 v82, v2
	v_mov_b32_e32 v83, v2
	v_mov_b32_e32 v84, v2
	v_mov_b32_e32 v85, v2
	v_mov_b32_e32 v90, v2
	v_mov_b32_e32 v91, v2
	v_mov_b32_e32 v92, v2
	v_mov_b32_e32 v93, v2
	v_mov_b32_e32 v98, v2
	v_mov_b32_e32 v99, v2
	v_mov_b32_e32 v100, v2
	v_mov_b32_e32 v101, v2
	v_mov_b32_e32 v106, v2
	v_mov_b32_e32 v107, v2
	v_mov_b32_e32 v108, v2
	v_mov_b32_e32 v109, v2
	v_mov_b32_e32 v122, v2
	v_mov_b32_e32 v123, v2
	v_mov_b32_e32 v124, v2
	v_mov_b32_e32 v125, v2
	v_mov_b32_e32 v138, v2
	v_mov_b32_e32 v139, v2
	v_mov_b32_e32 v140, v2
	v_mov_b32_e32 v141, v2
	v_mov_b32_e32 v70, v2
	v_mov_b32_e32 v71, v2
	v_mov_b32_e32 v72, v2
	v_mov_b32_e32 v73, v2
	v_mov_b32_e32 v78, v2
	v_mov_b32_e32 v79, v2
	v_mov_b32_e32 v80, v2
	v_mov_b32_e32 v81, v2
	v_mov_b32_e32 v86, v2
	v_mov_b32_e32 v87, v2
	v_mov_b32_e32 v88, v2
	v_mov_b32_e32 v89, v2
	v_mov_b32_e32 v94, v2
	v_mov_b32_e32 v95, v2
	v_mov_b32_e32 v96, v2
	v_mov_b32_e32 v97, v2
	v_mov_b32_e32 v102, v2
	v_mov_b32_e32 v103, v2
	v_mov_b32_e32 v104, v2
	v_mov_b32_e32 v105, v2
	v_mov_b32_e32 v114, v2
	v_mov_b32_e32 v115, v2
	v_mov_b32_e32 v116, v2
	v_mov_b32_e32 v117, v2
	v_mov_b32_e32 v134, v2
	v_mov_b32_e32 v135, v2
	v_mov_b32_e32 v136, v2
	v_mov_b32_e32 v137, v2
	v_mov_b32_e32 v142, v2
	v_mov_b32_e32 v143, v2
	v_mov_b32_e32 v144, v2
	v_mov_b32_e32 v145, v2
	s_cmp_gt_u32 s56, 1
	s_cselect_b32 s32, -2, 1
	s_waitcnt vmcnt(7)
	s_branch .LBB0_1085

; #define LAS __attribute__((address_space(3)))
; DI const char* sptr(const char* p) { const unsigned long long v = (unsigned long long)p; const unsigned lo = __builtin_amdgcn_readfirstlane((unsigned)v), hi = __builtin_amdgcn_readfirstlane((unsigned)(v >> 32)); return (const char*)(((unsigned long long)hi << 32) | lo); }
; template <class Epi, bool GATHER, bool EXPERT, bool FP8>
; DI void gemm_phase(LAS unsigned char* lds, const Gemm g, const StaticOrder& S, const Epi& E) {
;     ...
;         const char* nA = sptr(has_next ? (const char*)g.A + (GATHER ? (size_t)0 : (size_t)nxt.pm * tstep) : cA);
;         const char* nB = sptr(has_next ? (const char*)g.Bt + (size_t)nxt.e * g.estride + (size_t)nxt.pn * tstep : cB);
;         if (GATHER && has_next) {
;             int t2_ = threadIdx.x; asm volatile("" : "+v"(t2_));
; #pragma unroll
;             for (int i_ = 0; i_ < 2; ++i_) { int R_, C_; stage_rc(t2_ * 16 + i_ * 8192, R_, C_);
; #pragma unroll
;                 for (int h_ = 0; h_ < 2; ++h_) __builtin_amdgcn_global_load_lds((const unsigned*)(g.rowtok + nxt.pm * 256 + h_ * 128 + R_), (LAS unsigned*)(stash + (h_ * 2 + i_) * 2048), 4, 0, 0); }
;         }
;         int C0x2 = 0, C1x2 = 0; const LAS unsigned* sp = nullptr;
;         if (GATHER) { int t2_ = threadIdx.x; asm volatile("" : "+v"(t2_)); int R0_, C0_, R1_, C1_; stage_rc(t2_ * 16, R0_, C0_); stage_rc(t2_ * 16 + 8192, R1_, C1_); C0x2 = C0_ * 2; C1x2 = C1_ * 2;
;             sp = (const LAS unsigned*)(stash + (t2_ & 63) * 4); }
;         asm volatile(".p2align 8" ::: "memory");
; #pragma unroll 1
;         for (int t = 0; t < nt; t += 2) {
;             const bool last = (t == nt - 2);
;             const char* a1 = cA + (size_t)(t + 1) * kstep;
;             const char* a2 = last ? nA : cA + (size_t)(t + 2) * kstep; const char* b2 = last ? nB : cB + (size_t)(t + 2) * kstep;
;             const char* a3 = a2 + kstep; const char* b3 = b2 + kstep;
;     ...
;         for (int a = 0; a < 2; ++a)
; #pragma unroll
;             for (int b = 0; b < 2; ++b)
; #pragma unroll
;                 for (int m = 0; m < 4; ++m)
; #pragma unroll
;                     for (int n = 0; n < 2; ++n) acc[a][b][m][n] = (f32x4){0.f, 0.f, 0.f, 0.f};
.LBB0_1160:
	s_ashr_i32 s23, s22, 31
	s_lshl_b64 s[0:1], s[22:23], 19
	s_add_u32 s21, s19, s0
	s_addc_u32 s23, s40, s1
	s_and_b64 s[0:1], s[4:5], exec
	s_cselect_b32 s24, s21, s34
	s_cselect_b32 s25, s23, s35
	s_lshl_b64 s[0:1], s[26:27], 22
	s_add_u32 s23, s41, s0
	s_addc_u32 s33, s42, s1
	s_ashr_i32 s21, s20, 31
	s_lshl_b64 s[0:1], s[20:21], 19
	s_add_u32 s21, s23, s0
	s_addc_u32 s23, s33, s1
	s_and_b64 s[0:1], s[4:5], exec
	s_cselect_b32 s4, s21, s36
	s_cselect_b32 s5, s23, s37
	s_add_u32 s0, s36, 0x100
	.p2align 8
	s_addc_u32 s1, s37, 0
	s_add_u32 s34, s34, 0x80
	v_mov_b32_e32 v0, 0
	s_addc_u32 s35, s35, 0
	s_mov_b32 s21, -2
	v_mov_b32_e32 v1, v0
	v_mov_b32_e32 v2, v0
	v_mov_b32_e32 v3, v0
	v_mov_b32_e32 v4, v0
	v_mov_b32_e32 v5, v0
	v_mov_b32_e32 v6, v0
	v_mov_b32_e32 v7, v0
	v_mov_b32_e32 v8, v0
	v_mov_b32_e32 v9, v0
	v_mov_b32_e32 v10, v0
	v_mov_b32_e32 v11, v0
	v_mov_b32_e32 v12, v0
	v_mov_b32_e32 v13, v0
	v_mov_b32_e32 v14, v0
	v_mov_b32_e32 v15, v0
	v_mov_b32_e32 v32, v0
	v_mov_b32_e32 v33, v0
	v_mov_b32_e32 v34, v0
	v_mov_b32_e32 v35, v0
	v_mov_b32_e32 v36, v0
	v_mov_b32_e32 v37, v0
	v_mov_b32_e32 v38, v0
	v_mov_b32_e32 v39, v0
	v_mov_b32_e32 v40, v0
	v_mov_b32_e32 v41, v0
	v_mov_b32_e32 v42, v0
	v_mov_b32_e32 v43, v0
	v_mov_b32_e32 v44, v0
	v_mov_b32_e32 v45, v0
	v_mov_b32_e32 v46, v0
	v_mov_b32_e32 v47, v0
	v_mov_b32_e32 v16, v0
	v_mov_b32_e32 v17, v0
	v_mov_b32_e32 v18, v0
	v_mov_b32_e32 v19, v0
	v_mov_b32_e32 v20, v0
	v_mov_b32_e32 v21, v0
	v_mov_b32_e32 v22, v0
	v_mov_b32_e32 v23, v0
	v_mov_b32_e32 v24, v0
	v_mov_b32_e32 v25, v0
	v_mov_b32_e32 v26, v0
	v_mov_b32_e32 v27, v0
	v_mov_b32_e32 v28, v0
	v_mov_b32_e32 v29, v0
	v_mov_b32_e32 v30, v0
	v_mov_b32_e32 v31, v0
	v_mov_b32_e32 v48, v0
	v_mov_b32_e32 v49, v0
	v_mov_b32_e32 v50, v0
	v_mov_b32_e32 v51, v0
	v_mov_b32_e32 v52, v0
	v_mov_b32_e32 v53, v0
	v_mov_b32_e32 v54, v0
	v_mov_b32_e32 v55, v0
	v_mov_b32_e32 v56, v0
	v_mov_b32_e32 v57, v0
	v_mov_b32_e32 v58, v0
	v_mov_b32_e32 v59, v0
	v_mov_b32_e32 v60, v0
	v_mov_b32_e32 v61, v0
	v_mov_b32_e32 v62, v0
	v_mov_b32_e32 v63, v0
	v_mov_b32_e32 v64, v0
	v_mov_b32_e32 v65, v0
	v_mov_b32_e32 v66, v0
	v_mov_b32_e32 v67, v0
	v_mov_b32_e32 v68, v0
	v_mov_b32_e32 v69, v0
	v_mov_b32_e32 v70, v0
	v_mov_b32_e32 v71, v0
	v_mov_b32_e32 v72, v0
	v_mov_b32_e32 v73, v0
	v_mov_b32_e32 v74, v0
	v_mov_b32_e32 v75, v0
	v_mov_b32_e32 v76, v0
	v_mov_b32_e32 v77, v0
	v_mov_b32_e32 v78, v0
	v_mov_b32_e32 v79, v0
	v_mov_b32_e32 v96, v0
	v_mov_b32_e32 v97, v0
	v_mov_b32_e32 v98, v0
	v_mov_b32_e32 v99, v0
	v_mov_b32_e32 v100, v0
	v_mov_b32_e32 v101, v0
	v_mov_b32_e32 v102, v0
	v_mov_b32_e32 v103, v0
	v_mov_b32_e32 v104, v0
	v_mov_b32_e32 v105, v0
	v_mov_b32_e32 v106, v0
	v_mov_b32_e32 v107, v0
	v_mov_b32_e32 v108, v0
	v_mov_b32_e32 v109, v0
	v_mov_b32_e32 v110, v0
	v_mov_b32_e32 v111, v0
	v_mov_b32_e32 v80, v0
	v_mov_b32_e32 v81, v0
	v_mov_b32_e32 v82, v0
	v_mov_b32_e32 v83, v0
	v_mov_b32_e32 v84, v0
	v_mov_b32_e32 v85, v0
	v_mov_b32_e32 v86, v0
	v_mov_b32_e32 v87, v0
	v_mov_b32_e32 v88, v0
	v_mov_b32_e32 v89, v0
	v_mov_b32_e32 v90, v0
	v_mov_b32_e32 v91, v0
	v_mov_b32_e32 v92, v0
	v_mov_b32_e32 v93, v0
	v_mov_b32_e32 v94, v0
	v_mov_b32_e32 v95, v0
	v_mov_b32_e32 v112, v0
	v_mov_b32_e32 v113, v0
	v_mov_b32_e32 v114, v0
	v_mov_b32_e32 v115, v0
	v_mov_b32_e32 v116, v0
	v_mov_b32_e32 v117, v0
	v_mov_b32_e32 v118, v0
	v_mov_b32_e32 v119, v0
	v_mov_b32_e32 v120, v0
	v_mov_b32_e32 v121, v0
	v_mov_b32_e32 v122, v0
	v_mov_b32_e32 v123, v0
	v_mov_b32_e32 v124, v0
	v_mov_b32_e32 v125, v0
	v_mov_b32_e32 v126, v0
	v_mov_b32_e32 v127, v0
	s_cmp_gt_u32 s61, 1
	s_cselect_b32 s32, -2, 1
	s_waitcnt vmcnt(11)
